# GLA chunk: o tile converted f32->e4m3 in registers and stored directly (4 dword stores/wave), removing the bf16 LDS round trip, the write-out block and one barrier per chunk
# speedup vs baseline: 1.0051x; 1.0051x over previous
.LBB0_463:
	s_andn2_b64 vcc, exec, s[0:1]
	s_cbranch_vccnz .LBB0_748
	v_writelane_b32 v255, s86, 39
	s_movk_i32 s1, 0x800
	s_cmpk_gt_i32 s20, 0xff
	v_writelane_b32 v255, s87, 40
	v_writelane_b32 v255, s82, 43
	v_writelane_b32 v255, s94, 44
	s_cbranch_scc1 .LBB0_493
	s_add_u32 s78, s76, 0x46600000
	s_addc_u32 s79, s77, 0
	s_add_u32 s80, s76, 0x15e00000
	s_addc_u32 s81, s77, 0
	s_lshl_b32 s82, s71, 3
	s_or_b32 s84, s82, 1
	s_sub_i32 s83, 0xff, s82
	s_sub_i32 s85, 0xff, s84
	s_lshl_b32 s86, s71, 8
	s_cmp_gt_i32 s71, 0
	s_waitcnt lgkmcnt(0)
	s_cselect_b64 s[42:43], -1, 0
	s_cmp_gt_i32 s71, 1
	s_cselect_b64 s[44:45], -1, 0
	s_cmp_gt_i32 s71, 2
	s_waitcnt vmcnt(0)
	v_ashrrev_i32_e32 v17, 3, v126
	s_cselect_b64 s[46:47], -1, 0
	s_cmp_gt_i32 s71, 3
	v_and_b32_e32 v86, 0x7f, v126
	v_and_b32_e32 v87, -16, v17
	v_lshl_add_u32 v91, v127, 2, 0
	v_lshlrev_b32_e32 v3, 1, v127
	s_cselect_b64 s[48:49], -1, 0
	s_cmp_gt_i32 s71, 4
	v_and_b32_e32 v1, 15, v126
	v_lshrrev_b32_e32 v2, 4, v127
	v_sub_u32_e32 v92, v91, v3
	v_mul_u32_u24_e32 v3, 0x90, v86
	v_lshlrev_b32_e32 v4, 1, v87
	s_cselect_b64 s[50:51], -1, 0
	s_cmp_gt_i32 s71, 5
	s_movk_i32 s0, 0x8e
	v_add3_u32 v94, 0, v3, v4
	v_lshlrev_b32_e32 v4, 3, v2
	v_lshlrev_b32_e32 v2, 2, v2
	v_lshlrev_b32_e32 v6, 4, v126
	v_mul_u32_u24_e32 v100, 0x90, v1
	s_cselect_b64 s[52:53], -1, 0
	s_cmp_gt_i32 s71, 6
	v_mad_u32_u24 v93, v127, s0, v92
	v_sub_u32_e32 v2, v1, v2
	v_and_b32_e32 v76, 0x70, v6
	s_movk_i32 s0, 0x110
	v_add3_u32 v101, 0, v100, v4
	s_cselect_b64 s[54:55], -1, 0
	s_cmp_gt_i32 s71, 7
	v_and_b32_e32 v5, 48, v127
	v_mul_lo_u32 v6, v17, s0
	v_lshlrev_b32_e32 v7, 1, v76
	v_cmp_gt_i32_e32 vcc, 0, v2
	v_cmp_gt_i32_e64 s[58:59], 1, v2
	v_cmp_gt_i32_e64 s[62:63], 2, v2
	v_cmp_gt_i32_e64 s[40:41], 3, v2
	v_lshlrev_b32_e32 v2, 7, v1
	v_add_u32_e32 v103, 0x1200, v101
	s_movk_i32 s0, 0x1000
	s_cselect_b64 s[56:57], -1, 0
	s_lshl_b32 s87, s71, 4
	v_add_u32_e32 v95, 0, v5
	v_add3_u32 v96, 0, v6, v7
	v_mul_u32_u24_e32 v6, 0x48, v1
	v_add_u32_e32 v102, 0x900, v101
	v_add3_u32 v8, v103, v2, s0
	v_add_u32_e32 v104, 0x1b00, v101
	s_movk_i32 s0, 0x1800
	s_cmp_lt_u32 s16, 64
	v_lshl_add_u32 v97, v6, 1, v95
	v_add_u32_e32 v6, v101, v2
	v_add3_u32 v7, v102, v2, s1
	v_add3_u32 v2, v104, v2, s0
	s_cselect_b64 s[18:19], -1, 0
	v_or_b32_e32 v1, s87, v1
	s_movk_i32 s0, 0x90
	s_and_b64 s[62:63], s[40:41], s[62:63]
	v_or_b32_e32 v89, 1, v87
	v_mul_i32_i24_e32 v3, 0xffffff74, v127
	v_and_b32_e32 v5, 48, v126
	v_mul_lo_u32 v105, v1, s0
	s_lshl_b32 s0, s71, 5
	s_and_b64 s[72:73], s[62:63], s[58:59]
	v_sub_u32_e32 v88, 0xff, v87
	v_sub_u32_e32 v90, 0xff, v89
	v_mov_b32_e32 v77, v34
	v_add_u32_e32 v98, 0x1200, v97
	v_add_u32_e32 v99, 0x1b00, v97
	v_add3_u32 v106, 0, v105, v4
	v_sub_u32_e32 v107, 0, v17
	v_lshrrev_b32_e32 v218, 4, v127
	v_lshl_add_u32 v218, v218, 2, s87
	s_sub_i32 s16, 0, s82
	v_sub_u32_e32 v108, 0, v87
	v_add_u32_e32 v109, v93, v3
	v_add_u32_e32 v110, s0, v6
	v_add_u32_e32 v111, s0, v7
	v_add_u32_e32 v112, s0, v8
	v_add_u32_e32 v113, s0, v2
	v_add_u32_e32 v114, 0, v5
	s_and_b64 s[2:3], s[72:73], vcc
	s_mov_b32 s17, s20
	s_branch .LBB0_467

.LBB0_467:
	s_bfe_u32 s0, s17, 0x50002
	s_and_b32 s36, s17, 3
	s_lshl_b32 s1, s17, 1
	s_and_b32 s37, s1, 0x7fffff00
	s_lshl_b32 s1, s36, 7
	s_lshl_b32 s88, s0, 8
	s_cmpk_lt_u32 s17, 0x80
	s_cselect_b64 s[58:59], -1, 0
	s_and_b64 s[14:15], s[58:59], exec
	v_lshl_or_b32 v2, s36, 6, v127
	s_mov_b32 s14, 0x38600000
	v_lshlrev_b32_e32 v78, 1, v2
	v_or_b32_e32 v2, s37, v2
	s_cselect_b32 s15, s82, s83
	s_cselect_b32 s37, s84, s85
	s_cselect_b32 s14, s14, 0x3ce00000
	s_add_i32 s36, s88, s15
	s_add_i32 s64, s88, s37
	s_sub_i32 s94, s64, s36
	s_ashr_i32 s37, s36, 31
	s_mul_i32 s90, s36, 0x1800
	s_mul_hi_i32 s65, s36, 0x1800
	s_add_u32 s90, s90, s80
	s_addc_u32 s91, s65, s81
	s_lshl_b64 s[92:93], s[36:37], 10
	s_add_u32 s92, s92, s78
	s_addc_u32 s93, s93, s79
	v_lshlrev_b32_e32 v80, 1, v2
	global_load_ushort v115, v78, s[90:91]
	global_load_ushort v116, v78, s[90:91] offset:512
	global_load_ushort v117, v80, s[92:93]
	s_ashr_i32 s65, s64, 31
	s_mul_i32 s90, s64, 0x1800
	s_mul_hi_i32 s37, s64, 0x1800
	s_add_u32 s90, s90, s80
	s_addc_u32 s91, s37, s81
	s_lshl_b64 s[64:65], s[64:65], 10
	s_add_u32 s64, s64, s78
	s_addc_u32 s65, s65, s79
	s_lshl_b32 s37, s94, 1
	s_add_i32 s36, s37, s36
	global_load_ushort v118, v78, s[90:91]
	global_load_ushort v119, v78, s[90:91] offset:512
	global_load_ushort v120, v80, s[64:65]
	s_ashr_i32 s37, s36, 31
	s_mul_i32 s64, s36, 0x1800
	s_mul_hi_i32 s65, s36, 0x1800
	s_add_u32 s64, s64, s80
	s_addc_u32 s65, s65, s81
	s_lshl_b64 s[90:91], s[36:37], 10
	s_add_u32 s90, s90, s78
	s_addc_u32 s91, s91, s79
	s_add_i32 s36, s36, s94
	global_load_ushort v121, v78, s[64:65]
	global_load_ushort v122, v78, s[64:65] offset:512
	global_load_ushort v123, v80, s[90:91]
	s_ashr_i32 s37, s36, 31
	s_mul_i32 s64, s36, 0x1800
	s_mul_hi_i32 s65, s36, 0x1800
	s_add_u32 s64, s64, s80
	s_addc_u32 s65, s65, s81
	s_lshl_b64 s[90:91], s[36:37], 10
	s_add_u32 s90, s90, s78
	s_addc_u32 s91, s91, s79
	s_add_i32 s36, s36, s94
	global_load_ushort v124, v78, s[64:65]
	global_load_ushort v125, v78, s[64:65] offset:512
	global_load_ushort v128, v80, s[90:91]
	s_ashr_i32 s37, s36, 31
	s_mul_i32 s64, s36, 0x1800
	s_mul_hi_i32 s65, s36, 0x1800
	s_add_u32 s64, s64, s80
	s_addc_u32 s65, s65, s81
	s_lshl_b64 s[90:91], s[36:37], 10
	s_add_u32 s90, s90, s78
	s_addc_u32 s91, s91, s79
	s_add_i32 s36, s36, s94
	global_load_ushort v129, v78, s[64:65]
	global_load_ushort v130, v78, s[64:65] offset:512
	global_load_ushort v131, v80, s[90:91]
	s_ashr_i32 s37, s36, 31
	s_mul_i32 s64, s36, 0x1800
	s_mul_hi_i32 s65, s36, 0x1800
	s_add_u32 s64, s64, s80
	s_addc_u32 s65, s65, s81
	s_lshl_b64 s[90:91], s[36:37], 10
	s_add_u32 s90, s90, s78
	s_addc_u32 s91, s91, s79
	s_add_i32 s36, s36, s94
	global_load_ushort v132, v78, s[64:65]
	global_load_ushort v133, v78, s[64:65] offset:512
	global_load_ushort v134, v80, s[90:91]
	s_ashr_i32 s37, s36, 31
	s_mul_i32 s64, s36, 0x1800
	s_mul_hi_i32 s65, s36, 0x1800
	s_add_u32 s64, s64, s80
	s_addc_u32 s65, s65, s81
	s_lshl_b64 s[90:91], s[36:37], 10
	s_add_u32 s90, s90, s78
	s_addc_u32 s91, s91, s79
	s_add_i32 s36, s36, s94
	global_load_ushort v135, v78, s[64:65]
	global_load_ushort v136, v78, s[64:65] offset:512
	global_load_ushort v137, v80, s[90:91]
	s_ashr_i32 s37, s36, 31
	s_mul_i32 s64, s36, 0x1800
	s_mul_hi_i32 s65, s36, 0x1800
	s_add_u32 s64, s64, s80
	s_addc_u32 s65, s65, s81
	s_lshl_b64 s[36:37], s[36:37], 10
	s_add_u32 s36, s36, s78
	v_cndmask_b32_e64 v1, v88, v87, s[58:59]
	v_cndmask_b32_e64 v3, v90, v89, s[58:59]
	s_addc_u32 s37, s37, s79
	v_add_u32_e32 v1, s88, v1
	v_add_u32_e32 v3, s88, v3
	global_load_ushort v138, v78, s[64:65]
	global_load_ushort v139, v78, s[64:65] offset:512
	global_load_ushort v140, v80, s[36:37]
	v_readfirstlane_b32 s15, v3
	v_readfirstlane_b32 s64, v1
	s_sub_i32 s90, s15, s64
	s_mul_i32 s36, s64, 0x1800
	s_mul_hi_i32 s37, s64, 0x1800
	s_add_u32 s36, s36, s80
	v_or_b32_e32 v2, s1, v86
	s_addc_u32 s37, s37, s81
	v_lshl_or_b32 v82, v2, 1, v239
	global_load_ushort v2, v82, s[36:37]
	s_mul_hi_i32 s37, s15, 0x1800
	s_mulk_i32 s15, 0x1800
	s_add_u32 s36, s15, s80
	s_addc_u32 s37, s37, s81
	s_lshl_b32 s15, s90, 1
	s_add_i32 s15, s15, s64
	global_load_ushort v1, v82, s[36:37]
	s_mul_i32 s36, s15, 0x1800
	s_mul_hi_i32 s37, s15, 0x1800
	s_add_u32 s36, s36, s80
	s_addc_u32 s37, s37, s81
	s_add_i32 s15, s15, s90
	global_load_ushort v4, v82, s[36:37]
	s_mul_i32 s36, s15, 0x1800
	s_mul_hi_i32 s37, s15, 0x1800
	s_add_u32 s36, s36, s80
	s_addc_u32 s37, s37, s81
	s_add_i32 s15, s15, s90
	global_load_ushort v3, v82, s[36:37]
	s_mul_i32 s36, s15, 0x1800
	s_mul_hi_i32 s37, s15, 0x1800
	s_add_u32 s36, s36, s80
	s_addc_u32 s37, s37, s81
	s_add_i32 s15, s15, s90
	global_load_ushort v6, v82, s[36:37]
	s_mul_i32 s36, s15, 0x1800
	s_mul_hi_i32 s37, s15, 0x1800
	s_add_u32 s36, s36, s80
	s_addc_u32 s37, s37, s81
	s_add_i32 s15, s15, s90
	global_load_ushort v5, v82, s[36:37]
	s_mul_i32 s36, s15, 0x1800
	s_mul_hi_i32 s37, s15, 0x1800
	s_add_u32 s36, s36, s80
	s_addc_u32 s37, s37, s81
	s_add_i32 s15, s15, s90
	global_load_ushort v8, v82, s[36:37]
	s_mul_i32 s36, s15, 0x1800
	s_mul_hi_i32 s37, s15, 0x1800
	s_add_u32 s36, s36, s80
	s_addc_u32 s37, s37, s81
	s_add_i32 s15, s15, s90
	global_load_ushort v7, v82, s[36:37]
	s_mul_i32 s36, s15, 0x1800
	s_mul_hi_i32 s37, s15, 0x1800
	s_add_u32 s36, s36, s80
	s_addc_u32 s37, s37, s81
	s_add_i32 s15, s15, s90
	global_load_ushort v10, v82, s[36:37]
	s_mul_i32 s36, s15, 0x1800
	s_mul_hi_i32 s37, s15, 0x1800
	s_add_u32 s36, s36, s80
	s_addc_u32 s37, s37, s81
	s_add_i32 s15, s15, s90
	global_load_ushort v9, v82, s[36:37]
	s_mul_i32 s36, s15, 0x1800
	s_mul_hi_i32 s37, s15, 0x1800
	s_add_u32 s36, s36, s80
	s_addc_u32 s37, s37, s81
	s_add_i32 s15, s15, s90
	global_load_ushort v12, v82, s[36:37]
	s_mul_i32 s36, s15, 0x1800
	s_mul_hi_i32 s37, s15, 0x1800
	s_add_u32 s36, s36, s80
	s_addc_u32 s37, s37, s81
	s_add_i32 s15, s15, s90
	global_load_ushort v11, v82, s[36:37]
	s_mul_i32 s36, s15, 0x1800
	s_mul_hi_i32 s37, s15, 0x1800
	s_add_u32 s36, s36, s80
	s_addc_u32 s37, s37, s81
	s_add_i32 s15, s15, s90
	s_mul_i32 s64, s15, 0x1800
	s_mul_hi_i32 s65, s15, 0x1800
	s_add_u32 s64, s64, s80
	s_addc_u32 s65, s65, s81
	s_add_i32 s15, s15, s90
	global_load_ushort v14, v82, s[36:37]
	s_mul_i32 s36, s15, 0x1800
	s_mul_hi_i32 s37, s15, 0x1800
	s_add_u32 s36, s36, s80
	s_addc_u32 s37, s37, s81
	s_add_i32 s15, s15, s90
	global_load_ushort v13, v82, s[64:65]
	s_mul_hi_i32 s65, s15, 0x1800
	s_mulk_i32 s15, 0x1800
	s_add_u32 s64, s15, s80
	s_addc_u32 s65, s65, s81
	global_load_ushort v16, v82, s[36:37]
	global_load_ushort v15, v82, s[64:65]
	s_add_u32 s14, s76, s14
	s_addc_u32 s15, s77, 0
	s_lshl_b32 s90, s0, 11
	s_addk_i32 s90, 0x2000
	s_add_u32 s0, s14, s1
	s_addc_u32 s1, s15, 0
	s_waitcnt vmcnt(0)
	v_mov_b32_e32 v18, 0
	s_mov_b32 s89, 0
	v_mov_b32_e32 v79, v34
	v_mov_b32_e32 v81, v34
	v_mov_b32_e32 v83, v34
	s_mov_b32 s91, 0
	s_mov_b32 s92, 0
	v_mov_b32_e32 v19, v18
	v_mov_b32_e32 v20, v18
	v_mov_b32_e32 v21, v18
	v_mov_b32_e32 v22, v18
	v_mov_b32_e32 v23, v18
	v_mov_b32_e32 v24, v18
	v_mov_b32_e32 v25, v18
	v_mov_b32_e32 v26, v18
	v_mov_b32_e32 v27, v18
	v_mov_b32_e32 v28, v18
	v_mov_b32_e32 v29, v18
	v_mov_b32_e32 v36, v18
	v_mov_b32_e32 v37, v18
	v_mov_b32_e32 v38, v18
	v_mov_b32_e32 v39, v18
	v_lshl_add_u64 v[84:85], s[0:1], 0, v[76:77]
	s_mov_b64 s[94:95], s[0:1]
	s_barrier
	s_branch .LBB0_469
.LBB0_468:
	s_add_i32 s91, s91, 64
	s_sub_i32 s89, s89, 64
	s_add_i32 s92, s92, 1
	s_cmpk_eq_i32 s91, 0x900
	s_waitcnt vmcnt(41)
	s_waitcnt vmcnt(38)
	s_waitcnt vmcnt(35)
	s_waitcnt vmcnt(32)
	s_waitcnt vmcnt(29)
	s_waitcnt vmcnt(26)
	s_waitcnt vmcnt(23)
	s_waitcnt vmcnt(20)
	s_waitcnt vmcnt(19)
	s_waitcnt vmcnt(18)
	s_waitcnt vmcnt(17)
	s_waitcnt vmcnt(16)
	s_waitcnt vmcnt(15)
	s_waitcnt vmcnt(14)
	s_waitcnt vmcnt(13)
	s_waitcnt vmcnt(12)
	s_waitcnt vmcnt(11)
	s_waitcnt vmcnt(10)
	s_waitcnt vmcnt(9)
	s_waitcnt vmcnt(8)
	s_waitcnt vmcnt(7)
	s_waitcnt vmcnt(6)
	s_waitcnt vmcnt(5)
	s_waitcnt vmcnt(4)
	v_mov_b32_e32 v1, v219
	v_mov_b32_e32 v2, v220
	v_mov_b32_e32 v3, v221
	v_mov_b32_e32 v4, v222
	v_mov_b32_e32 v5, v223
	v_mov_b32_e32 v6, v224
	v_mov_b32_e32 v7, v225
	v_mov_b32_e32 v8, v226
	v_mov_b32_e32 v9, v227
	v_mov_b32_e32 v10, v228
	v_mov_b32_e32 v11, v229
	v_mov_b32_e32 v12, v230
	v_mov_b32_e32 v13, v231
	v_mov_b32_e32 v14, v232
	v_mov_b32_e32 v15, v233
	v_mov_b32_e32 v16, v246
	v_mov_b32_e32 v115, v178
	v_mov_b32_e32 v116, v179
	v_mov_b32_e32 v117, v180
	v_mov_b32_e32 v118, v181
	v_mov_b32_e32 v119, v182
	v_mov_b32_e32 v120, v183
	v_mov_b32_e32 v121, v184
	v_mov_b32_e32 v122, v185
	v_mov_b32_e32 v123, v186
	v_mov_b32_e32 v124, v187
	v_mov_b32_e32 v125, v188
	v_mov_b32_e32 v128, v189
	v_mov_b32_e32 v129, v190
	v_mov_b32_e32 v130, v192
	v_mov_b32_e32 v131, v194
	v_mov_b32_e32 v132, v196
	v_mov_b32_e32 v133, v200
	v_mov_b32_e32 v134, v201
	v_mov_b32_e32 v135, v202
	v_mov_b32_e32 v136, v203
	v_mov_b32_e32 v137, v206
	v_mov_b32_e32 v138, v207
	v_mov_b32_e32 v139, v208
	v_mov_b32_e32 v140, v209
	s_cbranch_scc1 .LBB0_466

.LBB0_486:
	s_waitcnt lgkmcnt(0)
	s_barrier
	v_and_b32_e32 v176, 15, v127
	v_add_u32_e32 v177, s91, v176
	v_sub_u32_e32 v176, s89, v176
	s_mov_b32 s0, 0x2000
	s_movk_i32 s1, 0x4000
	s_cmp_gt_u32 s92, 3
	s_cbranch_scc0 .Lgo_ctx
	v_add_u32_e32 v215, 0xffffff00, v177
	v_add_u32_e32 v216, 0x8ff, v176
	v_cndmask_b32_e64 v215, v216, v215, s[58:59]
	v_lshlrev_b32_e32 v216, 6, v215
	v_and_b32_e32 v216, 0x7c0, v216
	v_ashrrev_i32_e32 v251, 5, v215
	v_add_u32_e32 v216, v216, v251
	v_cndmask_b32_e64 v215, v216, v215, s[38:39]
	v_add_u32_e32 v215, s90, v215
	s_bitcmp1_b32 s38, 0
	s_cbranch_scc1 .Lgo_row
	s_mov_b32 s0, 0x80000
	s_movk_i32 s1, 0x200
	s_branch .Lgo_row
.Lgo_ctx:
	v_add_u32_e32 v215, 0xff, v176
	v_cndmask_b32_e64 v215, v215, v177, s[58:59]
	v_add_u32_e32 v215, s88, v215
.Lgo_row:
	s_bitcmp1_b32 s58, 0
	s_cbranch_scc1 .Lgo_pos
	s_sub_i32 s0, 0, s0
	s_sub_i32 s1, 0, s1
.Lgo_pos:
	v_lshl_add_u32 v251, v215, 9, v218
	v_add_u32_e32 v252, s0, v251
	v_add_u32_e32 v253, s1, v251
	v_add_u32_e32 v216, s1, v252
	ds_read_b128 v[30:33], v97 offset:9216
	ds_read_b128 v[40:43], v97 offset:9280
	ds_read_b128 v[44:47], v97 offset:11520
	ds_read_b128 v[52:55], v97 offset:2304
	ds_read_b128 v[60:63], v97 offset:11584
	ds_read_b128 v[64:67], v97 offset:2368
	ds_read_b128 v[72:75], v98 offset:9216
	ds_read_b128 v[142:145], v98
	ds_read_b128 v[146:149], v98 offset:9280
	ds_read_b128 v[150:153], v98 offset:64
	ds_read_b128 v[154:157], v99 offset:9216
	ds_read_b128 v[158:161], v99
	ds_read_b128 v[162:165], v99 offset:9280
	ds_read_b128 v[166:169], v99 offset:64
	ds_read_b128 v[48:51], v97 offset:64
	ds_read_b128 v[56:59], v97
	s_waitcnt lgkmcnt(0)
	v_mfma_f32_16x16x32_bf16 v[56:59], v[30:33], v[56:59], 0
	v_mfma_f32_16x16x32_bf16 v[48:51], v[40:43], v[48:51], v[56:59]
	s_nop 7
	v_cndmask_b32_e64 v35, v51, 0, s[40:41]
	v_cndmask_b32_e64 v141, v50, 0, s[62:63]
	v_cndmask_b32_e64 v170, v49, 0, s[72:73]
	v_cndmask_b32_e64 v171, v48, 0, s[2:3]
	v_mfma_f32_16x16x32_bf16 v[48:51], v[30:33], v[52:55], 0
	v_mfma_f32_16x16x32_bf16 v[56:59], v[40:43], v[64:67], v[48:51]
	v_mfma_f32_16x16x32_bf16 v[48:51], v[30:33], v[142:145], 0
	v_mfma_f32_16x16x32_bf16 v[30:33], v[30:33], v[158:161], 0
	v_mfma_f32_16x16x32_bf16 v[48:51], v[40:43], v[150:153], v[48:51]
	v_mfma_f32_16x16x32_bf16 v[40:43], v[40:43], v[166:169], v[30:33]
	v_mfma_f32_16x16x32_bf16 v[30:33], v[44:47], v[52:55], 0
	v_mfma_f32_16x16x32_bf16 v[30:33], v[60:63], v[64:67], v[30:33]
	v_cvt_pk_bf16_f32 v64, v26, v27
	v_cvt_pk_bf16_f32 v65, v28, v29
	v_cvt_pk_bf16_f32 v66, v36, v37
	v_cvt_pk_bf16_f32 v67, v38, v39
	s_nop 3
	v_cndmask_b32_e64 v172, v33, 0, s[40:41]
	v_cndmask_b32_e64 v173, v32, 0, s[62:63]
	v_cndmask_b32_e64 v174, v31, 0, s[72:73]
	v_cndmask_b32_e64 v175, v30, 0, s[2:3]
	v_mfma_f32_16x16x32_bf16 v[30:33], v[44:47], v[142:145], 0
	v_mfma_f32_16x16x32_bf16 v[68:71], v[60:63], v[150:153], v[30:33]
	v_mfma_f32_16x16x32_bf16 v[30:33], v[44:47], v[158:161], 0
	v_mfma_f32_16x16x32_bf16 v[52:55], v[60:63], v[166:169], v[30:33]
	v_cvt_pk_bf16_f32 v60, v18, v19
	v_cvt_pk_bf16_f32 v61, v20, v21
	v_cvt_pk_bf16_f32 v62, v22, v23
	v_mfma_f32_16x16x32_bf16 v[30:33], v[72:75], v[142:145], 0
	v_cvt_pk_bf16_f32 v63, v24, v25
	v_mfma_f32_16x16x32_bf16 v[30:33], v[146:149], v[150:153], v[30:33]
	s_nop 7
	v_cndmask_b32_e64 v150, v33, 0, s[40:41]
	v_cndmask_b32_e64 v151, v32, 0, s[62:63]
	v_cndmask_b32_e64 v152, v31, 0, s[72:73]
	v_cndmask_b32_e64 v153, v30, 0, s[2:3]
	v_mfma_f32_16x16x32_bf16 v[30:33], v[72:75], v[158:161], 0
	v_mfma_f32_16x16x32_bf16 v[44:47], v[146:149], v[166:169], v[30:33]
	v_mfma_f32_16x16x32_bf16 v[30:33], v[154:157], v[158:161], 0
	v_mfma_f32_16x16x32_bf16 v[30:33], v[162:165], v[166:169], v[30:33]
	s_nop 7
	v_cndmask_b32_e64 v157, v30, 0, s[2:3]
	v_add_u32_e32 v30, 0x6800, v106
	ds_read2_b64 v[142:145], v30 offset0:128 offset1:132
	ds_read2_b64 v[72:75], v30 offset0:136 offset1:140
	v_cndmask_b32_e64 v154, v33, 0, s[40:41]
	v_cndmask_b32_e64 v155, v32, 0, s[62:63]
	v_cvt_pk_bf16_f32 v32, v171, v170
	v_cvt_pk_bf16_f32 v33, v141, v35
	v_mov_b32_e32 v35, v34
	ds_read2_b64 v[146:149], v101 offset1:4
	v_cndmask_b32_e64 v156, v31, 0, s[72:73]
	s_waitcnt lgkmcnt(2)
	v_mfma_f32_16x16x32_bf16 v[30:33], v[142:145], v[32:35], 0
	s_waitcnt lgkmcnt(0)
	v_mfma_f32_16x16x32_bf16 v[30:33], v[60:63], v[146:149], v[30:33]
	ds_read2_b64 v[146:149], v101 offset0:8 offset1:12
	s_waitcnt lgkmcnt(0)
	v_mfma_f32_16x16x32_bf16 v[30:33], v[64:67], v[146:149], v[30:33]
	s_nop 7
	v_mul_f32_e32 v30, 4.0, v30
	v_mul_f32_e32 v31, 4.0, v31
	v_mul_f32_e32 v32, 4.0, v32
	v_mul_f32_e32 v33, 4.0, v33
	v_med3_f32 v30, v30, s75, v238
	v_med3_f32 v31, v31, s75, v238
	v_med3_f32 v32, v32, s75, v238
	v_med3_f32 v33, v33, s75, v238
	v_cvt_pk_fp8_f32 v247, v30, v31
	s_nop 1
	v_cvt_pk_fp8_f32 v247, v32, v33 op_sel:[0,0,1]
	s_nop 1
	global_store_dword v251, v247, s[94:95]
	v_cvt_pk_bf16_f32 v30, v56, v57
	v_cvt_pk_bf16_f32 v31, v58, v59
	v_cvt_pk_bf16_f32 v32, v175, v174
	v_cvt_pk_bf16_f32 v33, v173, v172
	ds_read2_b64 v[56:59], v102 offset1:4
	s_nop 0
	v_mfma_f32_16x16x32_bf16 v[30:33], v[142:145], v[30:33], 0
	s_waitcnt lgkmcnt(0)
	v_mfma_f32_16x16x32_bf16 v[30:33], v[60:63], v[56:59], v[30:33]
	ds_read2_b64 v[56:59], v102 offset0:8 offset1:12
	s_waitcnt lgkmcnt(0)
	v_mfma_f32_16x16x32_bf16 v[30:33], v[64:67], v[56:59], v[30:33]
	s_nop 7
	v_mul_f32_e32 v30, 4.0, v30
	v_mul_f32_e32 v31, 4.0, v31
	v_mul_f32_e32 v32, 4.0, v32
	v_mul_f32_e32 v33, 4.0, v33
	v_med3_f32 v30, v30, s75, v238
	v_med3_f32 v31, v31, s75, v238
	v_med3_f32 v32, v32, s75, v238
	v_med3_f32 v33, v33, s75, v238
	v_cvt_pk_fp8_f32 v248, v30, v31
	s_nop 1
	v_cvt_pk_fp8_f32 v248, v32, v33 op_sel:[0,0,1]
	s_nop 1
	global_store_dword v252, v248, s[94:95]
	v_cvt_pk_bf16_f32 v30, v48, v49
	v_cvt_pk_bf16_f32 v31, v50, v51
	v_cvt_pk_bf16_f32 v32, v68, v69
	v_cvt_pk_bf16_f32 v33, v70, v71
	s_nop 1
	v_mfma_f32_16x16x32_bf16 v[48:51], v[142:145], v[30:33], 0
	v_cvt_pk_bf16_f32 v32, v153, v152
	v_cvt_pk_bf16_f32 v33, v151, v150
	s_nop 1
	v_mfma_f32_16x16x32_bf16 v[30:33], v[72:75], v[32:35], v[48:51]
	v_add_u32_e32 v35, v95, v105
	s_nop 1
	ds_read2_b64 v[48:51], v103 offset1:4
	s_waitcnt lgkmcnt(0)
	v_mfma_f32_16x16x32_bf16 v[30:33], v[60:63], v[48:51], v[30:33]
	ds_read2_b64 v[48:51], v103 offset0:8 offset1:12
	s_waitcnt lgkmcnt(0)
	v_mfma_f32_16x16x32_bf16 v[30:33], v[64:67], v[48:51], v[30:33]
	s_nop 7
	v_mul_f32_e32 v30, 4.0, v30
	v_mul_f32_e32 v31, 4.0, v31
	v_mul_f32_e32 v32, 4.0, v32
	v_mul_f32_e32 v33, 4.0, v33
	v_med3_f32 v30, v30, s75, v238
	v_med3_f32 v31, v31, s75, v238
	v_med3_f32 v32, v32, s75, v238
	v_med3_f32 v33, v33, s75, v238
	v_cvt_pk_fp8_f32 v249, v30, v31
	s_nop 1
	v_cvt_pk_fp8_f32 v249, v32, v33 op_sel:[0,0,1]
	s_nop 1
	global_store_dword v253, v249, s[94:95]
	v_cvt_pk_bf16_f32 v30, v40, v41
	v_cvt_pk_bf16_f32 v31, v42, v43
	v_cvt_pk_bf16_f32 v32, v52, v53
	v_cvt_pk_bf16_f32 v33, v54, v55
	v_cvt_pk_bf16_f32 v40, v44, v45
	v_cvt_pk_bf16_f32 v41, v46, v47
	v_mfma_f32_16x16x32_bf16 v[30:33], v[142:145], v[30:33], 0
	v_cvt_pk_bf16_f32 v42, v157, v156
	v_cvt_pk_bf16_f32 v43, v155, v154
	v_add_u32_e32 v44, v95, v100
	s_nop 0
	v_mfma_f32_16x16x32_bf16 v[30:33], v[72:75], v[40:43], v[30:33]
	ds_read2_b64 v[40:43], v104 offset1:4
	s_waitcnt lgkmcnt(0)
	v_mfma_f32_16x16x32_bf16 v[30:33], v[60:63], v[40:43], v[30:33]
	ds_read2_b64 v[40:43], v104 offset0:8 offset1:12
	s_waitcnt lgkmcnt(0)
	v_mfma_f32_16x16x32_bf16 v[30:33], v[64:67], v[40:43], v[30:33]
	s_nop 7
	v_mul_f32_e32 v30, 4.0, v30
	v_mul_f32_e32 v31, 4.0, v31
	v_mul_f32_e32 v32, 4.0, v32
	v_mul_f32_e32 v33, 4.0, v33
	v_med3_f32 v30, v30, s75, v238
	v_med3_f32 v31, v31, s75, v238
	v_med3_f32 v32, v32, s75, v238
	v_med3_f32 v33, v33, s75, v238
	v_cvt_pk_fp8_f32 v250, v30, v31
	s_nop 1
	v_cvt_pk_fp8_f32 v250, v32, v33 op_sel:[0,0,1]
	s_nop 1
	global_store_dword v216, v250, s[94:95]
	ds_read_b128 v[30:33], v114 offset:48128
	ds_read_b128 v[40:43], v44 offset:18432
	s_waitcnt lgkmcnt(1)
	v_pk_mul_f32 v[18:19], v[18:19], v[30:31]
	v_pk_mul_f32 v[20:21], v[20:21], v[32:33]
	ds_read_b128 v[30:33], v114 offset:48192
	s_waitcnt lgkmcnt(0)
	v_pk_mul_f32 v[22:23], v[22:23], v[30:31]
	v_pk_mul_f32 v[24:25], v[24:25], v[32:33]
	ds_read_b128 v[30:33], v114 offset:48256
	s_waitcnt lgkmcnt(0)
	v_pk_mul_f32 v[26:27], v[26:27], v[30:31]
	v_pk_mul_f32 v[28:29], v[28:29], v[32:33]
	ds_read_b128 v[30:33], v114 offset:48320
	s_waitcnt lgkmcnt(0)
	v_pk_mul_f32 v[30:31], v[36:37], v[30:31]
	v_pk_mul_f32 v[32:33], v[38:39], v[32:33]
	ds_read_b128 v[36:39], v35 offset:27648
	s_waitcnt lgkmcnt(0)
	v_mfma_f32_16x16x32_bf16 v[18:21], v[40:43], v[36:39], v[18:21]
	ds_read_b128 v[40:43], v44 offset:20736
	s_waitcnt lgkmcnt(0)
	v_mfma_f32_16x16x32_bf16 v[22:25], v[40:43], v[36:39], v[22:25]
	ds_read_b128 v[40:43], v44 offset:23040
	s_waitcnt lgkmcnt(0)
	v_mfma_f32_16x16x32_bf16 v[26:29], v[40:43], v[36:39], v[26:29]
	ds_read_b128 v[40:43], v44 offset:25344
	s_waitcnt lgkmcnt(0)
	v_mfma_f32_16x16x32_bf16 v[30:33], v[40:43], v[36:39], v[30:33]
	ds_read_b128 v[36:39], v35 offset:27712
	ds_read_b128 v[40:43], v44 offset:18496
	s_waitcnt lgkmcnt(0)
	v_mfma_f32_16x16x32_bf16 v[18:21], v[40:43], v[36:39], v[18:21]
	ds_read_b128 v[40:43], v44 offset:20800
	s_waitcnt lgkmcnt(0)
	v_mfma_f32_16x16x32_bf16 v[22:25], v[40:43], v[36:39], v[22:25]
	ds_read_b128 v[40:43], v44 offset:23104
	s_waitcnt lgkmcnt(0)
	v_mfma_f32_16x16x32_bf16 v[26:29], v[40:43], v[36:39], v[26:29]
	ds_read_b128 v[40:43], v44 offset:25408
	s_waitcnt lgkmcnt(0)
	v_mfma_f32_16x16x32_bf16 v[36:39], v[40:43], v[36:39], v[30:33]
	s_nop 2
	s_branch .LBB0_468
